# MLP2 prologue: compiler's full vmcnt(0) drain after staging K-tile 1 relaxed to vmcnt(5) (residual loads are older and complete)
# speedup vs baseline: 1.0079x; 1.0079x over previous
.LBB6_8:
	s_mov_b64 s[20:21], 0x80
	s_add_i32 s54, s47, 0xa000
	v_lshl_add_u64 v[24:25], v[24:25], 0, s[20:21]
	s_mov_b32 m0, s54
	s_add_i32 s55, s47, 0xc000
	s_waitcnt vmcnt(0)
	s_barrier
	global_load_lds_dwordx4 v[24:25], off
	v_lshl_add_u64 v[22:23], v[22:23], 0, s[20:21]
	s_mov_b32 m0, s55
	s_add_i32 s56, s47, 0xe000
	global_load_lds_dwordx4 v[22:23], off
	v_lshl_add_u64 v[20:21], v[20:21], 0, s[20:21]
	s_mov_b32 m0, s56
	v_lshl_add_u64 v[18:19], v[18:19], 0, s[20:21]
	global_load_lds_dwordx4 v[20:21], off
	s_add_i32 m0, s47, 0x10000
	v_lshl_add_u64 v[16:17], v[16:17], 0, s[20:21]
	global_load_lds_dwordx4 v[18:19], off
	s_add_i32 m0, s47, 0x12000
	v_or_b32_e32 v126, s28, v41
	global_load_lds_dwordx4 v[16:17], off
	s_waitcnt vmcnt(5)
	v_cvt_f32_f16_sdwa v101, v6 dst_sel:DWORD dst_unused:UNUSED_PAD src0_sel:WORD_1
	v_cvt_f32_f16_e32 v100, v6
	v_cvt_f32_f16_sdwa v103, v4 dst_sel:DWORD dst_unused:UNUSED_PAD src0_sel:WORD_1
	v_cvt_f32_f16_e32 v102, v4
	v_cvt_f32_f16_sdwa v105, v5 dst_sel:DWORD dst_unused:UNUSED_PAD src0_sel:WORD_1
	v_cvt_f32_f16_e32 v104, v5
	v_lshlrev_b32_e32 v4, 4, v40
	s_movk_i32 s0, 0x3c0
	v_lshlrev_b32_e32 v5, 6, v126
	v_lshlrev_b32_e32 v6, 2, v126
	v_and_or_b32 v5, v5, s0, v4
	s_lshl_b32 s1, s27, 13
	v_and_b32_e32 v6, 32, v6
	v_bitop3_b32 v127, v5, s1, v6 bitop3:0xde
	v_lshlrev_b32_e32 v5, 6, v0
	v_lshlrev_b32_e32 v0, 2, v0
	v_and_or_b32 v4, v5, s0, v4
	s_mulk_i32 s4, 0x1800
	v_and_b32_e32 v0, 32, v0
	v_bitop3_b32 v128, s4, v4, v0 bitop3:0xf6
	v_add_u32_e32 v0, v38, v3
	v_cvt_f32_f16_sdwa v85, v12 dst_sel:DWORD dst_unused:UNUSED_PAD src0_sel:WORD_1
	v_cvt_f32_f16_e32 v84, v12
	v_add_u32_e32 v3, v39, v3
	v_or_b32_e32 v12, 0x80, v0
	v_cvt_f32_f16_sdwa v87, v9 dst_sel:DWORD dst_unused:UNUSED_PAD src0_sel:WORD_1
	v_cvt_f32_f16_sdwa v89, v8 dst_sel:DWORD dst_unused:UNUSED_PAD src0_sel:WORD_1
	v_cvt_f32_f16_e32 v88, v8
	v_cvt_f32_f16_e32 v86, v9
	v_cvt_f32_f16_sdwa v95, v11 dst_sel:DWORD dst_unused:UNUSED_PAD src0_sel:WORD_1
	v_cvt_f32_f16_sdwa v97, v10 dst_sel:DWORD dst_unused:UNUSED_PAD src0_sel:WORD_1
	v_cvt_f32_f16_e32 v96, v10
	v_cvt_f32_f16_e32 v94, v11
	v_cvt_f32_f16_sdwa v99, v7 dst_sel:DWORD dst_unused:UNUSED_PAD src0_sel:WORD_1
	v_cvt_f32_f16_e32 v98, v7
	v_mad_u64_u32 v[4:5], s[0:1], s7, v0, v[2:3]
	v_mad_u64_u32 v[6:7], s[0:1], s26, v0, v[2:3]
	v_mad_u64_u32 v[8:9], s[0:1], s7, v3, v[2:3]
	v_mad_u64_u32 v[10:11], s[0:1], s26, v3, v[2:3]
	v_mad_u64_u32 v[2:3], s[0:1], s26, v12, v[2:3]
	s_ashr_i32 s0, s6, 31
	s_lshr_b32 s0, s0, 26
	s_add_i32 s0, s6, s0
	v_cvt_f32_f16_sdwa v59, v37 dst_sel:DWORD dst_unused:UNUSED_PAD src0_sel:WORD_1
	v_cvt_f32_f16_sdwa v61, v36 dst_sel:DWORD dst_unused:UNUSED_PAD src0_sel:WORD_1
	v_cvt_f32_f16_e32 v60, v36
	v_cvt_f32_f16_e32 v58, v37
	v_cvt_f32_f16_sdwa v63, v35 dst_sel:DWORD dst_unused:UNUSED_PAD src0_sel:WORD_1
	v_cvt_f32_f16_sdwa v65, v34 dst_sel:DWORD dst_unused:UNUSED_PAD src0_sel:WORD_1
	v_cvt_f32_f16_e32 v64, v34
	v_cvt_f32_f16_e32 v62, v35
	v_cvt_f32_f16_sdwa v67, v33 dst_sel:DWORD dst_unused:UNUSED_PAD src0_sel:WORD_1
	v_cvt_f32_f16_sdwa v69, v32 dst_sel:DWORD dst_unused:UNUSED_PAD src0_sel:WORD_1
	v_cvt_f32_f16_e32 v68, v32
	v_cvt_f32_f16_e32 v66, v33
	v_cvt_f32_f16_sdwa v71, v29 dst_sel:DWORD dst_unused:UNUSED_PAD src0_sel:WORD_1
	v_cvt_f32_f16_sdwa v73, v28 dst_sel:DWORD dst_unused:UNUSED_PAD src0_sel:WORD_1
	v_cvt_f32_f16_e32 v72, v28
	v_cvt_f32_f16_e32 v70, v29
	v_cvt_f32_f16_sdwa v75, v31 dst_sel:DWORD dst_unused:UNUSED_PAD src0_sel:WORD_1
	v_cvt_f32_f16_sdwa v77, v30 dst_sel:DWORD dst_unused:UNUSED_PAD src0_sel:WORD_1
	v_cvt_f32_f16_e32 v76, v30
	v_cvt_f32_f16_e32 v74, v31
	v_cvt_f32_f16_sdwa v79, v27 dst_sel:DWORD dst_unused:UNUSED_PAD src0_sel:WORD_1
	v_cvt_f32_f16_sdwa v81, v26 dst_sel:DWORD dst_unused:UNUSED_PAD src0_sel:WORD_1
	v_cvt_f32_f16_e32 v80, v26
	v_cvt_f32_f16_e32 v78, v27
	v_cvt_f32_f16_sdwa v83, v13 dst_sel:DWORD dst_unused:UNUSED_PAD src0_sel:WORD_1
	v_cvt_f32_f16_e32 v82, v13
	v_cvt_f32_f16_sdwa v91, v15 dst_sel:DWORD dst_unused:UNUSED_PAD src0_sel:WORD_1
	v_cvt_f32_f16_sdwa v93, v14 dst_sel:DWORD dst_unused:UNUSED_PAD src0_sel:WORD_1
	v_cvt_f32_f16_e32 v92, v14
	v_cvt_f32_f16_e32 v90, v15
	s_ashr_i32 s59, s0, 6
	v_add_lshl_u32 v0, v4, v1, 1
	v_add_lshl_u32 v4, v8, v1, 1
	v_add_lshl_u32 v6, v6, v1, 1
	v_add_lshl_u32 v8, v10, v1, 1
	v_add_lshl_u32 v2, v2, v1, 1
	s_cmp_gt_i32 s6, 63
	v_mov_b32_e32 v1, v49
	s_mov_b64 s[0:1], 0x100
	s_cselect_b64 s[6:7], -1, 0
	v_lshl_add_u64 v[106:107], v[0:1], 0, s[0:1]
	v_mov_b32_e32 v5, v49
	v_mov_b32_e32 v7, v49
	v_mov_b32_e32 v9, v49
	v_mov_b32_e32 v3, v49
	s_add_i32 s62, 0, 0x14000
	v_add_u32_e32 v0, 0x4000, v128
	v_or_b32_e32 v129, s5, v42
	s_add_i32 s60, s59, -3
	s_waitcnt lgkmcnt(0)
	s_ashr_i32 s61, s52, 31
	v_lshl_add_u64 v[108:109], v[4:5], 0, s[0:1]
	v_lshl_add_u64 v[110:111], v[6:7], 0, s[0:1]
	v_lshl_add_u64 v[112:113], v[8:9], 0, s[0:1]
	v_lshl_add_u64 v[114:115], v[2:3], 0, s[0:1]
	v_add_u32_e32 v130, s62, v0
	s_barrier
	s_branch .LBB6_10
